# all 384 per-segment s_setprio flips of the GEMM loops deleted; one static s_setprio 1 for waves 4-7 at kernel entry for the whole kernel
# baseline (speedup 1.0000x reference)
_Z3fwd6Params:
	s_mov_b32 s14, s2
	s_add_u32 s2, s0, 0x118
	s_addc_u32 s3, s1, 0
	v_readfirstlane_b32 s81, v0
	s_cmp_gt_u32 s81, 0xff
	s_cbranch_scc0 .Lnoprio_k
	s_setprio 1
.Lnoprio_k:
	v_writelane_b32 v255, s2, 0
	v_cmp_gt_u32_e32 vcc, 4, v0
	s_nop 0
	v_writelane_b32 v255, s3, 1
	s_and_saveexec_b64 s[2:3], vcc
	v_lshl_add_u32 v1, v0, 2, 0
	v_add_u32_e32 v1, 0x20000, v1
	v_mov_b32_e32 v2, 0
	ds_write_b32 v1, v2
	s_or_b64 exec, exec, s[2:3]
	s_load_dwordx2 s[34:35], s[0:1], 0x108
	s_mov_b32 s33, 0
	v_cmp_eq_u32_e32 vcc, 0, v0
	s_and_saveexec_b64 s[2:3], vcc
	s_cbranch_execz .LBB0_4
	s_load_dwordx16 s[16:31], s[0:1], 0x0
	s_add_i32 s4, 0, 0x20400
	s_load_dwordx16 s[36:51], s[0:1], 0x40
	v_mov_b32_e32 v4, s4
	s_add_i32 s4, 0, 0x20410
	s_waitcnt lgkmcnt(0)
	v_mov_b32_e32 v0, s16
	v_mov_b32_e32 v1, s17
	v_mov_b32_e32 v2, s18
	v_mov_b32_e32 v3, s19
	ds_write_b128 v4, v[0:3]
	v_mov_b32_e32 v0, s20
	v_mov_b32_e32 v1, s21
	v_mov_b32_e32 v2, s22
	v_mov_b32_e32 v3, s23
	v_mov_b32_e32 v4, s4
	s_add_i32 s4, 0, 0x20420
	ds_write_b128 v4, v[0:3]
	v_mov_b32_e32 v0, s24
	v_mov_b32_e32 v1, s25
	v_mov_b32_e32 v2, s26
	v_mov_b32_e32 v3, s27
	v_mov_b32_e32 v4, s4
	s_add_i32 s4, 0, 0x20430
	ds_write_b128 v4, v[0:3]
	v_mov_b32_e32 v0, s28
	v_mov_b32_e32 v1, s29
	v_mov_b32_e32 v2, s30
	v_mov_b32_e32 v3, s31
	v_mov_b32_e32 v4, s4
	s_add_i32 s4, 0, 0x20440
	s_load_dwordx16 s[16:31], s[0:1], 0x80
	ds_write_b128 v4, v[0:3]
	v_mov_b32_e32 v0, s36
	v_mov_b32_e32 v1, s37
	v_mov_b32_e32 v2, s38
	v_mov_b32_e32 v3, s39
	v_mov_b32_e32 v4, s4
	s_add_i32 s4, 0, 0x20450
	ds_write_b128 v4, v[0:3]
	v_mov_b32_e32 v0, s40
	v_mov_b32_e32 v1, s41
	v_mov_b32_e32 v2, s42
	v_mov_b32_e32 v3, s43
	v_mov_b32_e32 v4, s4
	s_add_i32 s4, 0, 0x20460
	ds_write_b128 v4, v[0:3]
	v_mov_b32_e32 v0, s44
	v_mov_b32_e32 v1, s45
	v_mov_b32_e32 v2, s46
	v_mov_b32_e32 v3, s47
	v_mov_b32_e32 v4, s4
	s_add_i32 s4, 0, 0x20470
	ds_write_b128 v4, v[0:3]
	v_mov_b32_e32 v0, s48
	v_mov_b32_e32 v1, s49
	v_mov_b32_e32 v2, s50
	v_mov_b32_e32 v3, s51
	v_mov_b32_e32 v4, s4
	s_add_i32 s4, 0, 0x20480
	s_load_dwordx16 s[36:51], s[0:1], 0xc0
	ds_write_b128 v4, v[0:3]
	s_waitcnt lgkmcnt(0)
	v_mov_b32_e32 v0, s16
	v_mov_b32_e32 v1, s17
	v_mov_b32_e32 v2, s18
	v_mov_b32_e32 v3, s19
	v_mov_b32_e32 v4, s4
	s_add_i32 s4, 0, 0x20490
	ds_write_b128 v4, v[0:3]
	v_mov_b32_e32 v0, s20
	v_mov_b32_e32 v1, s21
	v_mov_b32_e32 v2, s22
	v_mov_b32_e32 v3, s23
	v_mov_b32_e32 v4, s4
	s_add_i32 s4, 0, 0x204a0
	ds_write_b128 v4, v[0:3]
	v_mov_b32_e32 v0, s24
	v_mov_b32_e32 v1, s25
	v_mov_b32_e32 v2, s26
	v_mov_b32_e32 v3, s27
	v_mov_b32_e32 v4, s4
	s_add_i32 s4, 0, 0x204b0
	ds_write_b128 v4, v[0:3]
	v_mov_b32_e32 v0, s28
	v_mov_b32_e32 v1, s29
	v_mov_b32_e32 v2, s30
	v_mov_b32_e32 v3, s31
	v_mov_b32_e32 v4, s4
	s_add_i32 s4, 0, 0x204c0
	ds_write_b128 v4, v[0:3]
	v_mov_b32_e32 v0, s36
	v_mov_b32_e32 v1, s37
	v_mov_b32_e32 v2, s38
	v_mov_b32_e32 v3, s39
	v_mov_b32_e32 v4, s4
	s_add_i32 s4, 0, 0x204d0
	ds_write_b128 v4, v[0:3]
	v_mov_b32_e32 v0, s40
	v_mov_b32_e32 v1, s41
	v_mov_b32_e32 v2, s42
	v_mov_b32_e32 v3, s43
	v_mov_b32_e32 v4, s4
	s_add_i32 s4, 0, 0x204e0
	ds_write_b128 v4, v[0:3]
	v_mov_b32_e32 v4, s4
	s_load_dwordx2 s[4:5], s[0:1], 0x100
	v_mov_b32_e32 v0, s44
	v_mov_b32_e32 v1, s45
	v_mov_b32_e32 v2, s46
	v_mov_b32_e32 v3, s47
	s_add_i32 s6, 0, 0x204f0
	ds_write_b128 v4, v[0:3]
	v_mov_b32_e32 v0, s48
	v_mov_b32_e32 v1, s49
	v_mov_b32_e32 v2, s50
	v_mov_b32_e32 v3, s51
	v_mov_b32_e32 v4, s6
	s_add_i32 s6, 0, 0x20500
	ds_write_b128 v4, v[0:3]
	v_mov_b32_e32 v0, s6
	s_waitcnt lgkmcnt(0)
	v_mov_b64_e32 v[2:3], s[4:5]
	ds_write_b64 v0, v[2:3]

.LBB0_544:
	s_cmp_gt_i32 s36, 6
	s_cselect_b64 s[0:1], -1, 0
	s_cmp_lt_i32 s37, 7
	s_cselect_b64 s[2:3], -1, 0
	v_writelane_b32 v255, s80, 2
	s_or_b64 s[0:1], s[0:1], s[2:3]
	v_writelane_b32 v255, s81, 3
	s_and_b64 vcc, exec, s[0:1]
	v_writelane_b32 v255, s82, 4
	s_cbranch_vccnz .LBB0_895
	v_mbcnt_hi_u32_b32 v193, -1, v253
	s_and_b32 s0, s81, 0xffffffc0
	v_add_u32_e32 v184, s0, v193
	s_cmp_gt_u32 s81, 0xff
	s_cbranch_scc0 .Lnoprio_a0
.Lnoprio_a0:
	s_mov_b32 s46, s15
	s_mov_b64 s[6:7], s[34:35]
	s_mov_b32 s41, s14
	s_add_i32 s0, 0, 0x20468
	s_add_u32 s8, s6, 0x58000
	v_mov_b32_e32 v0, s0
	s_addc_u32 s9, s7, 0
	s_add_i32 s0, 0, 0x204a0
	s_waitcnt lgkmcnt(0)
	v_mov_b32_e32 v2, s0
	s_add_i32 s0, 0, 0x20488
	s_waitcnt vmcnt(0)
	v_mov_b32_e32 v4, s0
	ds_read_b64 v[0:1], v0
	ds_read_b64 v[2:3], v2
	ds_read_b64 v[4:5], v4
	v_readfirstlane_b32 s47, v184
	s_cmpk_lt_i32 s41, 0x110
	s_cselect_b64 s[12:13], -1, 0
	s_and_b32 s0, s47, 0xffffffc0
	s_mov_b32 s16, 0
	s_waitcnt lgkmcnt(2)
	v_readfirstlane_b32 s10, v0
	v_readfirstlane_b32 s11, v1
	s_waitcnt lgkmcnt(1)
	v_readfirstlane_b32 s48, v2
	v_readfirstlane_b32 s49, v3
	s_waitcnt lgkmcnt(0)
	v_readfirstlane_b32 s38, v4
	v_readfirstlane_b32 s39, v5
	s_cmpk_gt_i32 s41, 0x10f
	v_add_u32_e32 v200, s0, v193
	s_cbranch_scc1 .LBB0_598
	s_add_u32 s50, s6, 0x4619c000
	s_addc_u32 s51, s7, 0
	s_add_u32 s52, s6, 0x49d1c000
	s_addc_u32 s53, s7, 0
	s_add_u32 s54, s6, 0x216b8000
	s_addc_u32 s55, s7, 0
	s_add_u32 s56, s6, 0x37e0c000
	s_addc_u32 s57, s7, 0
	s_movk_i32 s58, 0xff
	s_movk_i32 s59, 0x100
	s_movk_i32 s60, 0x2000
	s_movk_i32 s61, 0xc00
	v_mov_b32_e32 v187, 0
	v_mov_b32_e32 v185, 0x358637bd
	s_mov_b32 s62, 0x800000
	s_mov_b32 s63, 0x2aaaaaab
	s_movk_i32 s64, 0x600
	s_movk_i32 s65, 0xd0
	s_movk_i32 s66, 0x50
	s_add_i32 s67, 0, 0x10000
	s_mov_b32 s68, 0xaaaaaaab
	s_mov_b32 s69, 0xc3e00000
	v_mov_b32_e32 v201, 0x7149f2ca
	s_mov_b32 s40, 0x3dd53b94
	s_mov_b32 s70, 0x41000000
	v_mov_b32_e32 v202, 0xc0a00000
	v_mov_b32_e32 v203, 0x43e00000
	v_mov_b32_e32 v204, 0xf149f2ca
	s_mov_b32 s71, s41
	s_branch .LBB0_548

.LBB0_1859:
	s_cmp_gt_i32 s36, 19
	s_cselect_b64 s[0:1], -1, 0
	s_cmp_lt_i32 s37, 20
	s_cselect_b64 s[2:3], -1, 0
	s_or_b64 s[0:1], s[0:1], s[2:3]
	s_and_b64 vcc, exec, s[0:1]
	s_cbranch_vccnz .LBB0_2175
	v_mbcnt_hi_u32_b32 v195, -1, v253
	s_and_b32 s0, s81, 0xffffffc0
	s_cmp_gt_u32 s81, 0xff
	s_cbranch_scc0 .Lnoprio_a1
.Lnoprio_a1:
	v_add_u32_e32 v184, s0, v195
	s_mov_b64 s[6:7], s[34:35]
	s_mov_b32 s44, s14
	s_mov_b32 s42, s15
	s_add_i32 s0, 0, 0x20468
	s_add_u32 s8, s6, 0x58000
	v_mov_b32_e32 v0, s0
	s_addc_u32 s9, s7, 0
	s_add_i32 s0, 0, 0x204a0
	s_waitcnt lgkmcnt(0)
	v_mov_b32_e32 v2, s0
	s_add_i32 s0, 0, 0x20488
	s_waitcnt vmcnt(0)
	v_mov_b32_e32 v4, s0
	ds_read_b64 v[0:1], v0
	ds_read_b64 v[2:3], v2
	ds_read_b64 v[4:5], v4
	v_readfirstlane_b32 s45, v184
	s_cmpk_lt_i32 s44, 0x100
	s_cselect_b64 s[12:13], -1, 0
	s_and_b32 s0, s45, 0xffffffc0
	s_mov_b32 s16, 0
	s_waitcnt lgkmcnt(2)
	v_readfirstlane_b32 s10, v0
	v_readfirstlane_b32 s11, v1
	s_waitcnt lgkmcnt(1)
	v_readfirstlane_b32 s46, v2
	v_readfirstlane_b32 s47, v3
	s_waitcnt lgkmcnt(0)
	v_readfirstlane_b32 s39, v4
	v_readfirstlane_b32 s43, v5
	s_movk_i32 s48, 0x100
	s_movk_i32 s49, 0xff
	s_cmpk_gt_i32 s44, 0xff
	v_add_u32_e32 v202, s0, v195
	s_cbranch_scc1 .LBB0_1899
	s_add_u32 s50, s6, 0x4619c000
	s_addc_u32 s51, s7, 0
	s_add_u32 s52, s6, 0x49d1c000
	s_addc_u32 s53, s7, 0
	s_add_u32 s54, s6, 0x216b8000
	s_addc_u32 s55, s7, 0
	s_add_u32 s56, s6, 0x37e0c000
	s_addc_u32 s57, s7, 0
	s_movk_i32 s58, 0xc00
	v_mov_b32_e32 v187, 0
	s_movk_i32 s59, 0x2000
	v_mov_b32_e32 v185, 0x358637bd
	s_mov_b32 s60, 0x800000
	s_mov_b32 s61, 0x2aaaaaab
	s_movk_i32 s62, 0x600
	s_movk_i32 s63, 0xd0
	s_movk_i32 s64, 0x50
	s_add_i32 s65, 0, 0x10000
	s_mov_b32 s66, 0xaaaaaaab
	s_mov_b32 s67, 0xc3e00000
	v_mov_b32_e32 v203, 0x7149f2ca
	s_mov_b32 s38, 0x3dd53b94
	s_mov_b32 s68, 0x41000000
	v_mov_b32_e32 v204, 0xc0a00000
	v_mov_b32_e32 v205, 0x43e00000
	v_mov_b32_e32 v206, 0xf149f2ca
	s_mov_b32 s69, s44
	s_branch .LBB0_1863
